# P9 row loads at system scope (sc0 sc1) beside the write-through output stores
# speedup vs baseline: 1.0112x; 1.0112x over previous
.LBB0_1205:
	s_add_i32 s1, s9, -3
	s_add_i32 s2, s9, -2
	s_add_i32 s3, s9, -1
	v_readlane_b32 s0, v130, s9
	v_readlane_b32 s24, v130, s1
	v_readlane_b32 s2, v130, s2
	v_readlane_b32 s26, v130, s3
	v_lshl_add_u64 v[0:1], s[92:93], 0, v[106:107]
	s_ashr_i32 s1, s0, 31
	s_ashr_i32 s25, s24, 31
	s_ashr_i32 s3, s2, 31
	s_ashr_i32 s27, s26, 31
	v_add_co_u32_e32 v0, vcc, s11, v0
	s_add_u32 s28, s92, s21
	v_mov_b32_e32 v6, 0
	v_addc_co_u32_e32 v1, vcc, 0, v1, vcc
	s_addc_u32 s29, s93, s22
	s_lshl_b64 s[24:25], s[24:25], 11
	v_lshl_add_u64 v[2:3], s[92:93], 0, v[110:111]
	v_lshl_add_u64 v[4:5], s[92:93], 0, v[108:109]
	s_lshl_b64 s[2:3], s[2:3], 11
	s_lshl_b64 s[26:27], s[26:27], 11
	s_lshl_b64 s[0:1], s[0:1], 11
	global_load_dwordx2 v[212:213], v126, s[28:29]
	global_load_dwordx4 v[132:135], v[0:1], off sc0 sc1
	global_load_dwordx4 v[136:139], v[2:3], off sc0 sc1
	global_load_dwordx4 v[140:143], v[0:1], off offset:2048 sc0 sc1
	global_load_dwordx4 v[144:147], v[4:5], off sc0 sc1
	v_lshl_add_u64 v[0:1], v[112:113], 0, s[24:25]
	v_lshl_add_u64 v[2:3], v[112:113], 0, s[2:3]
	v_lshl_add_u64 v[4:5], v[112:113], 0, s[26:27]
	v_lshl_add_u64 v[8:9], v[112:113], 0, s[0:1]
	global_load_dwordx4 v[92:95], v[0:1], off sc0 sc1
	global_load_dwordx4 v[88:91], v[2:3], off sc0 sc1
	global_load_dwordx4 v[84:87], v[4:5], off sc0 sc1
	global_load_dwordx4 v[80:83], v[8:9], off sc0 sc1
	global_load_dwordx4 v[76:79], v[0:1], off offset:1024 sc0 sc1
	global_load_dwordx4 v[72:75], v[2:3], off offset:1024 sc0 sc1
	global_load_dwordx4 v[68:71], v[4:5], off offset:1024 sc0 sc1
	global_load_dwordx4 v[64:67], v[8:9], off offset:1024 sc0 sc1
	v_lshl_add_u32 v44, v6, 2, v129
	ds_read_b128 v[148:151], v44
	ds_read_b128 v[152:155], v44 offset:1024
	ds_read_b128 v[156:159], v44 offset:8192
	ds_read_b128 v[160:163], v44 offset:9216
	ds_read_b128 v[164:167], v44 offset:2048
	ds_read_b128 v[168:171], v44 offset:3072
	ds_read_b128 v[172:175], v44 offset:10240
	ds_read_b128 v[176:179], v44 offset:11264
	ds_read_b128 v[180:183], v44 offset:4096
	ds_read_b128 v[184:187], v44 offset:5120
	ds_read_b128 v[188:191], v44 offset:12288
	ds_read_b128 v[192:195], v44 offset:13312
	ds_read_b128 v[196:199], v44 offset:6144
	ds_read_b128 v[200:203], v44 offset:7168
	ds_read_b128 v[204:207], v44 offset:14336
	ds_read_b128 v[208:211], v44 offset:15360
	ds_read_b128 v[16:19], v44 offset:16384
	ds_read_b128 v[0:3], v44 offset:17408
	ds_read_b128 v[48:51], v44 offset:24576
	ds_read_b128 v[32:35], v44 offset:25600
	ds_read_b128 v[20:23], v44 offset:18432
	ds_read_b128 v[4:7], v44 offset:19456
	ds_read_b128 v[52:55], v44 offset:26624
	ds_read_b128 v[36:39], v44 offset:27648
	ds_read_b128 v[24:27], v44 offset:20480
	ds_read_b128 v[8:11], v44 offset:21504
	ds_read_b128 v[56:59], v44 offset:28672
	ds_read_b128 v[40:43], v44 offset:29696
	ds_read_b128 v[28:31], v44 offset:22528
	ds_read_b128 v[12:15], v44 offset:23552
	ds_read_b128 v[60:63], v44 offset:30720
	ds_read_b128 v[44:47], v44 offset:31744
	s_add_u32 s4, s4, s6
	s_addc_u32 s5, s5, s7
	s_add_i32 s9, s9, 4
	s_add_u32 s21, s21, s12
	s_addc_u32 s22, s22, s13
	v_lshl_add_u64 v[116:117], s[16:17], 0, v[96:97]
	v_lshl_add_u64 v[118:119], s[16:17], 0, v[98:99]
	v_lshl_add_u64 v[120:121], s[16:17], 0, v[100:101]
	v_lshl_add_u64 v[122:123], s[16:17], 0, v[102:103]
	v_lshl_add_u64 v[124:125], s[16:17], 0, v[104:105]
	v_cmp_lt_u64_e32 vcc, s[4:5], v[114:115]
	s_add_u32 s16, s16, s18
	s_addc_u32 s17, s17, s19
	s_and_b64 s[0:1], exec, vcc
	v_lshl_add_u64 v[108:109], v[108:109], 0, s[14:15]
	v_lshl_add_u64 v[106:107], v[106:107], 0, s[14:15]
	v_lshl_add_u64 v[110:111], v[110:111], 0, s[14:15]
	s_waitcnt vmcnt(11)
	v_mov_b32_e32 v131, v134
	v_mov_b32_e32 v134, v135
	s_nop 0
	v_permlane16_swap_b32_e32 v132, v131
	s_waitcnt vmcnt(10)
	v_mov_b32_e32 v135, v138
	v_permlane16_swap_b32_e32 v133, v134
	s_waitcnt vmcnt(7)
	v_mov_b32_e32 v230, v93
	s_waitcnt vmcnt(2)
	v_mov_b32_e32 v235, v73
	s_waitcnt vmcnt(1)
	v_mov_b32_e32 v236, v69
	s_waitcnt vmcnt(0)
	v_mov_b32_e32 v237, v67
	v_lshlrev_b32_e32 v67, 16, v132
	v_and_b32_e32 v69, 0xffff0000, v132
	v_mov_b32_e32 v138, v139
	v_mov_b32_e32 v139, v142
	v_mov_b32_e32 v142, v143
	v_mov_b32_e32 v143, v146
	v_mov_b32_e32 v146, v147
	v_permlane16_swap_b32_e32 v136, v135
	v_mov_b32_e32 v231, v89
	v_mov_b32_e32 v234, v79
	v_lshlrev_b32_e32 v73, 16, v133
	v_and_b32_e32 v79, 0xffff0000, v133
	v_permlane16_swap_b32_e32 v92, v230
	v_permlane16_swap_b32_e32 v94, v95
	v_permlane16_swap_b32_e32 v72, v235
	v_sub_f32_e32 v133, v69, v212
	v_sub_f32_e32 v132, v67, v212
	v_permlane16_swap_b32_e32 v137, v138
	v_permlane16_swap_b32_e32 v140, v139
	v_permlane16_swap_b32_e32 v141, v142
	v_permlane16_swap_b32_e32 v144, v143
	v_permlane16_swap_b32_e32 v145, v146
	v_lshlrev_b32_e32 v89, 16, v134
	v_and_b32_e32 v93, 0xffff0000, v134
	v_lshlrev_b32_e32 v216, 16, v135
	v_and_b32_e32 v217, 0xffff0000, v135
	v_permlane16_swap_b32_e32 v88, v231
	v_permlane16_swap_b32_e32 v90, v91
	v_permlane16_swap_b32_e32 v68, v236
	v_permlane16_swap_b32_e32 v66, v237
	v_sub_f32_e32 v135, v79, v212
	v_sub_f32_e32 v134, v73, v212
	v_permlane32_swap_b32_e32 v230, v95
	v_mov_b32_e32 v250, v72
	v_pk_mul_f32 v[72:73], v[212:213], v[132:133] op_sel:[1,0]
	v_mov_b32_e32 v232, v87
	v_mov_b32_e32 v233, v83
	v_lshlrev_b32_e32 v83, 16, v131
	v_and_b32_e32 v87, 0xffff0000, v131
	v_lshlrev_b32_e32 v131, 16, v136
	v_and_b32_e32 v147, 0xffff0000, v136
	v_lshlrev_b32_e32 v214, 16, v137
	v_and_b32_e32 v215, 0xffff0000, v137
	v_lshlrev_b32_e32 v218, 16, v138
	v_and_b32_e32 v219, 0xffff0000, v138
	v_lshlrev_b32_e32 v220, 16, v140
	v_and_b32_e32 v221, 0xffff0000, v140
	v_lshlrev_b32_e32 v222, 16, v141
	v_and_b32_e32 v223, 0xffff0000, v141
	v_lshlrev_b32_e32 v224, 16, v139
	v_and_b32_e32 v225, 0xffff0000, v139
	v_lshlrev_b32_e32 v228, 16, v144
	v_and_b32_e32 v229, 0xffff0000, v144
	v_lshlrev_b32_e32 v238, 16, v145
	v_and_b32_e32 v239, 0xffff0000, v145
	v_lshlrev_b32_e32 v240, 16, v143
	v_and_b32_e32 v241, 0xffff0000, v143
	v_permlane32_swap_b32_e32 v231, v91
	v_mov_b32_e32 v251, v68
	v_pk_mul_f32 v[68:69], v[212:213], v[134:135] op_sel:[1,0]
	v_mov_b32_e32 v252, v66
	s_waitcnt lgkmcnt(14)
	v_pk_fma_f32 v[66:67], v[72:73], v[148:149], v[156:157]
	v_cvt_pk_f32_fp8_e32 v[72:73], v230
	v_lshlrev_b32_e32 v226, 16, v142
	v_and_b32_e32 v227, 0xffff0000, v142
	v_lshlrev_b32_e32 v242, 16, v146
	v_and_b32_e32 v243, 0xffff0000, v146
	v_permlane16_swap_b32_e32 v86, v232
	v_permlane16_swap_b32_e32 v82, v233
	v_permlane16_swap_b32_e32 v76, v77
	v_permlane16_swap_b32_e32 v78, v234
	v_sub_f32_e32 v137, v87, v212
	v_sub_f32_e32 v136, v83, v212
	v_sub_f32_e32 v141, v215, v212
	v_sub_f32_e32 v140, v214, v212
	v_sub_f32_e32 v143, v147, v212
	v_sub_f32_e32 v142, v131, v212
	v_sub_f32_e32 v145, v219, v212
	v_sub_f32_e32 v144, v218, v212
	v_sub_f32_e32 v147, v217, v212
	v_sub_f32_e32 v146, v216, v212
	v_sub_f32_e32 v215, v221, v212
	v_sub_f32_e32 v214, v220, v212
	v_sub_f32_e32 v217, v223, v212
	v_sub_f32_e32 v216, v222, v212
	v_sub_f32_e32 v219, v225, v212
	v_sub_f32_e32 v218, v224, v212
	v_sub_f32_e32 v223, v239, v212
	v_sub_f32_e32 v222, v238, v212
	v_sub_f32_e32 v225, v229, v212
	v_sub_f32_e32 v224, v228, v212
	v_sub_f32_e32 v229, v241, v212
	v_sub_f32_e32 v228, v240, v212
	v_mov_b32_e32 v131, v92
	v_pk_fma_f32 v[68:69], v[68:69], v[150:151], v[158:159]
	v_cvt_pk_f32_fp8_sdwa v[148:149], v230 src0_sel:WORD_1
	v_cvt_pk_f32_fp8_e32 v[158:159], v231
	v_permlane16_swap_b32_e32 v84, v85
	v_permlane16_swap_b32_e32 v80, v81
	v_permlane16_swap_b32_e32 v74, v75
	v_permlane16_swap_b32_e32 v70, v71
	v_permlane16_swap_b32_e32 v64, v65
	v_sub_f32_e32 v139, v93, v212
	v_sub_f32_e32 v138, v89, v212
	v_sub_f32_e32 v221, v227, v212
	v_sub_f32_e32 v220, v226, v212
	v_sub_f32_e32 v227, v243, v212
	v_sub_f32_e32 v226, v242, v212
	v_mov_b32_e32 v238, v88
	v_mov_b32_e32 v239, v86
	v_mov_b32_e32 v240, v82
	v_mov_b32_e32 v241, v78
	v_permlane32_swap_b32_e32 v77, v234
	v_pk_mul_f32 v[82:83], v[212:213], v[136:137] op_sel:[1,0]
	v_pk_mul_f32 v[92:93], v[212:213], v[146:147] op_sel:[1,0]
	v_pk_mul_f32 v[132:133], v[212:213], v[144:145] op_sel:[1,0]
	v_pk_mul_f32 v[136:137], v[212:213], v[214:215] op_sel:[1,0]
	v_pk_mul_f32 v[144:145], v[212:213], v[222:223] op_sel:[1,0]
	v_pk_mul_f32 v[146:147], v[212:213], v[228:229] op_sel:[1,0]
	v_permlane32_swap_b32_e32 v131, v94
	v_cvt_pk_f32_fp8_sdwa v[214:215], v231 src0_sel:WORD_1
	v_permlane32_swap_b32_e32 v85, v232
	v_permlane32_swap_b32_e32 v81, v233
	v_permlane32_swap_b32_e32 v235, v75
	v_permlane32_swap_b32_e32 v236, v71
	v_pk_mul_f32 v[78:79], v[212:213], v[138:139] op_sel:[1,0]
	v_pk_mul_f32 v[86:87], v[212:213], v[142:143] op_sel:[1,0]
	v_pk_mul_f32 v[88:89], v[212:213], v[140:141] op_sel:[1,0]
	v_pk_mul_f32 v[134:135], v[212:213], v[216:217] op_sel:[1,0]
	v_pk_mul_f32 v[138:139], v[212:213], v[220:221] op_sel:[1,0]
	v_pk_mul_f32 v[140:141], v[212:213], v[218:219] op_sel:[1,0]
	v_pk_mul_f32 v[142:143], v[212:213], v[224:225] op_sel:[1,0]
	v_pk_mul_f32 v[212:213], v[212:213], v[226:227] op_sel:[1,0]
	v_permlane32_swap_b32_e32 v65, v237
	v_cvt_pk_f32_fp8_e32 v[150:151], v95
	v_cvt_pk_f32_fp8_sdwa v[156:157], v95 src0_sel:WORD_1
	v_permlane32_swap_b32_e32 v238, v90
	v_permlane32_swap_b32_e32 v84, v239
	v_permlane32_swap_b32_e32 v80, v240
	v_permlane32_swap_b32_e32 v76, v241
	v_pk_fma_f32 v[132:133], v[132:133], v[170:171], v[178:179]
	v_pk_fma_f32 v[92:93], v[92:93], v[168:169], v[176:177]
	v_cvt_pk_f32_fp8_e32 v[168:169], v77
	v_cvt_pk_f32_fp8_sdwa v[170:171], v77 src0_sel:WORD_1
	v_cvt_pk_f32_fp8_e32 v[176:177], v234
	v_cvt_pk_f32_fp8_sdwa v[178:179], v234 src0_sel:WORD_1
	v_pk_fma_f32 v[144:145], v[144:145], v[198:199], v[206:207]
	v_pk_fma_f32 v[146:147], v[146:147], v[200:201], v[208:209]
	v_cvt_pk_f32_fp8_e32 v[198:199], v131
	v_cvt_pk_f32_fp8_sdwa v[200:201], v131 src0_sel:WORD_1
	v_pk_fma_f32 v[82:83], v[82:83], v[152:153], v[160:161]
	v_pk_fma_f32 v[78:79], v[78:79], v[154:155], v[162:163]
	v_cvt_pk_f32_fp8_e32 v[152:153], v91
	v_cvt_pk_f32_fp8_sdwa v[154:155], v91 src0_sel:WORD_1
	v_cvt_pk_f32_fp8_e32 v[216:217], v232
	v_pk_fma_f32 v[88:89], v[88:89], v[166:167], v[174:175]
	v_pk_fma_f32 v[86:87], v[86:87], v[164:165], v[172:173]
	v_cvt_pk_f32_fp8_sdwa v[164:165], v232 src0_sel:WORD_1
	v_cvt_pk_f32_fp8_e32 v[174:175], v233
	v_cvt_pk_f32_fp8_sdwa v[218:219], v233 src0_sel:WORD_1
	v_permlane32_swap_b32_e32 v250, v74
	v_cvt_pk_f32_fp8_e32 v[220:221], v235
	v_cvt_pk_f32_fp8_sdwa v[222:223], v235 src0_sel:WORD_1
	v_pk_fma_f32 v[136:137], v[136:137], v[180:181], v[188:189]
	v_pk_fma_f32 v[134:135], v[134:135], v[182:183], v[190:191]
	v_cvt_pk_f32_fp8_e32 v[180:181], v75
	v_cvt_pk_f32_fp8_sdwa v[182:183], v75 src0_sel:WORD_1
	v_cvt_pk_f32_fp8_e32 v[188:189], v236
	v_cvt_pk_f32_fp8_sdwa v[190:191], v236 src0_sel:WORD_1
	v_pk_fma_f32 v[138:139], v[138:139], v[186:187], v[194:195]
	v_cvt_pk_f32_fp8_e32 v[194:195], v237
	v_cvt_pk_f32_fp8_sdwa v[226:227], v237 src0_sel:WORD_1
	v_pk_fma_f32 v[142:143], v[142:143], v[196:197], v[204:205]
	v_pk_fma_f32 v[196:197], v[212:213], v[202:203], v[210:211]
	v_cvt_pk_f32_fp8_e32 v[202:203], v94
	v_cvt_pk_f32_fp8_sdwa v[94:95], v94 src0_sel:WORD_1
	v_cvt_pk_f32_fp8_e32 v[204:205], v238
	v_cvt_pk_f32_fp8_sdwa v[206:207], v238 src0_sel:WORD_1
	v_cvt_pk_f32_fp8_e32 v[212:213], v239
	v_cvt_pk_f32_fp8_sdwa v[228:229], v239 src0_sel:WORD_1
	v_cvt_pk_f32_fp8_e32 v[232:233], v240
	v_cvt_pk_f32_fp8_sdwa v[234:235], v240 src0_sel:WORD_1
	v_cvt_pk_f32_fp8_e32 v[236:237], v76
	v_cvt_pk_f32_fp8_sdwa v[76:77], v76 src0_sel:WORD_1
	v_cvt_pk_f32_fp8_e32 v[238:239], v241
	v_cvt_pk_f32_fp8_sdwa v[240:241], v241 src0_sel:WORD_1
	v_pk_add_f32 v[72:73], v[72:73], 0 op_sel_hi:[1,0]
	v_cvt_pk_f32_fp8_e32 v[160:161], v85
	v_cvt_pk_f32_fp8_sdwa v[162:163], v85 src0_sel:WORD_1
	v_permlane32_swap_b32_e32 v251, v70
	v_cvt_pk_f32_fp8_e32 v[224:225], v71
	v_pk_fma_f32 v[140:141], v[140:141], v[184:185], v[192:193]
	v_cvt_pk_f32_fp8_sdwa v[184:185], v71 src0_sel:WORD_1
	v_cvt_pk_f32_fp8_e32 v[208:209], v90
	v_cvt_pk_f32_fp8_sdwa v[90:91], v90 src0_sel:WORD_1
	v_cvt_pk_f32_fp8_e32 v[210:211], v84
	v_cvt_pk_f32_fp8_sdwa v[84:85], v84 src0_sel:WORD_1
	v_cvt_pk_f32_fp8_e32 v[242:243], v74
	v_cvt_pk_f32_fp8_sdwa v[74:75], v74 src0_sel:WORD_1
	v_cvt_pk_f32_fp8_e32 v[248:249], v250
	v_pk_add_f32 v[72:73], v[72:73], v[158:159]
	v_cvt_pk_f32_fp8_sdwa v[158:159], v250 src0_sel:WORD_1
	v_pk_add_f32 v[148:149], v[148:149], 0 op_sel_hi:[1,0]
	v_cvt_pk_f32_fp8_e32 v[166:167], v81
	v_cvt_pk_f32_fp8_sdwa v[172:173], v81 src0_sel:WORD_1
	v_permlane32_swap_b32_e32 v64, v252
	v_cvt_pk_f32_fp8_e32 v[186:187], v65
	v_cvt_pk_f32_fp8_sdwa v[192:193], v65 src0_sel:WORD_1
	v_cvt_pk_f32_fp8_e32 v[230:231], v80
	v_cvt_pk_f32_fp8_sdwa v[80:81], v80 src0_sel:WORD_1
	v_cvt_pk_f32_fp8_e32 v[244:245], v70
	v_cvt_pk_f32_fp8_sdwa v[70:71], v70 src0_sel:WORD_1
	v_pk_add_f32 v[148:149], v[148:149], v[214:215]
	v_cvt_pk_f32_fp8_e32 v[214:215], v251
	v_cvt_pk_f32_fp8_sdwa v[250:251], v251 src0_sel:WORD_1
	v_cvt_pk_f32_fp8_e32 v[246:247], v64
	v_cvt_pk_f32_fp8_sdwa v[64:65], v64 src0_sel:WORD_1
	v_pk_add_f32 v[150:151], v[150:151], 0 op_sel_hi:[1,0]
	v_pk_add_f32 v[156:157], v[156:157], 0 op_sel_hi:[1,0]
	v_pk_add_f32 v[168:169], v[168:169], 0 op_sel_hi:[1,0]
	v_pk_add_f32 v[170:171], v[170:171], 0 op_sel_hi:[1,0]
	v_pk_add_f32 v[176:177], v[176:177], 0 op_sel_hi:[1,0]
	v_pk_add_f32 v[178:179], v[178:179], 0 op_sel_hi:[1,0]
	v_pk_add_f32 v[198:199], v[198:199], 0 op_sel_hi:[1,0]
	v_pk_add_f32 v[200:201], v[200:201], 0 op_sel_hi:[1,0]
	v_pk_add_f32 v[150:151], v[150:151], v[152:153]
	v_pk_add_f32 v[154:155], v[156:157], v[154:155]
	v_pk_add_f32 v[202:203], v[202:203], 0 op_sel_hi:[1,0]
	v_pk_add_f32 v[94:95], v[94:95], 0 op_sel_hi:[1,0]
	v_pk_add_f32 v[236:237], v[236:237], 0 op_sel_hi:[1,0]
	v_pk_add_f32 v[76:77], v[76:77], 0 op_sel_hi:[1,0]
	v_pk_add_f32 v[240:241], v[240:241], 0 op_sel_hi:[1,0]
	v_pk_add_f32 v[168:169], v[168:169], v[220:221]
	v_pk_add_f32 v[170:171], v[170:171], v[222:223]
	v_pk_add_f32 v[176:177], v[176:177], v[180:181]
	v_pk_add_f32 v[178:179], v[178:179], v[182:183]
	v_pk_add_f32 v[180:181], v[198:199], v[204:205]
	v_pk_add_f32 v[182:183], v[200:201], v[206:207]
	v_pk_add_f32 v[198:199], v[202:203], v[208:209]
	v_pk_add_f32 v[90:91], v[94:95], v[90:91]
	v_pk_add_f32 v[72:73], v[72:73], v[160:161]
	v_pk_add_f32 v[94:95], v[148:149], v[162:163]
	v_pk_add_f32 v[148:149], v[150:151], v[216:217]
	v_pk_add_f32 v[150:151], v[154:155], v[164:165]
	v_pk_add_f32 v[154:155], v[236:237], v[248:249]
	v_pk_add_f32 v[76:77], v[76:77], v[158:159]
	v_pk_add_f32 v[74:75], v[240:241], v[74:75]
	v_pk_add_f32 v[160:161], v[168:169], v[188:189]
	v_pk_add_f32 v[162:163], v[170:171], v[190:191]
	v_pk_add_f32 v[164:165], v[176:177], v[224:225]
	v_pk_add_f32 v[168:169], v[178:179], v[184:185]
	v_pk_add_f32 v[170:171], v[180:181], v[210:211]
	v_pk_add_f32 v[84:85], v[182:183], v[84:85]
	v_pk_mul_f32 v[68:69], v[68:69], s[8:9] op_sel_hi:[1,0]
	v_pk_mul_f32 v[66:67], v[66:67], s[8:9] op_sel_hi:[1,0]
	v_pk_mul_f32 v[78:79], v[78:79], s[8:9] op_sel_hi:[1,0]
	v_pk_mul_f32 v[82:83], v[82:83], s[8:9] op_sel_hi:[1,0]
	v_pk_mul_f32 v[132:133], v[132:133], s[8:9] op_sel_hi:[1,0]
	v_pk_mul_f32 v[92:93], v[92:93], s[8:9] op_sel_hi:[1,0]
	v_pk_mul_f32 v[138:139], v[138:139], s[8:9] op_sel_hi:[1,0]
	v_pk_mul_f32 v[140:141], v[140:141], s[8:9] op_sel_hi:[1,0]
	v_pk_mul_f32 v[196:197], v[196:197], s[8:9] op_sel_hi:[1,0]
	v_pk_mul_f32 v[146:147], v[146:147], s[8:9] op_sel_hi:[1,0]
	v_pk_add_f32 v[176:177], v[198:199], v[212:213]
	v_pk_add_f32 v[72:73], v[72:73], v[166:167]
	v_pk_add_f32 v[94:95], v[94:95], v[172:173]
	v_pk_add_f32 v[148:149], v[148:149], v[174:175]
	v_pk_add_f32 v[150:151], v[150:151], v[218:219]
	v_pk_add_f32 v[154:155], v[154:155], v[214:215]
	v_pk_add_f32 v[76:77], v[76:77], v[250:251]
	v_pk_add_f32 v[70:71], v[74:75], v[70:71]
	v_pk_add_f32 v[74:75], v[160:161], v[186:187]
	v_pk_add_f32 v[160:161], v[162:163], v[192:193]
	v_pk_add_f32 v[162:163], v[164:165], v[194:195]
	v_pk_add_f32 v[164:165], v[168:169], v[226:227]
	v_pk_add_f32 v[166:167], v[170:171], v[230:231]
	v_pk_add_f32 v[80:81], v[84:85], v[80:81]
	v_cvt_pk_f32_fp8_e32 v[152:153], v252
	v_pk_mul_f32 v[86:87], v[86:87], s[8:9] op_sel_hi:[1,0]
	v_pk_mul_f32 v[134:135], v[134:135], s[8:9] op_sel_hi:[1,0]
	v_pk_mul_f32 v[136:137], v[136:137], s[8:9] op_sel_hi:[1,0]
	v_pk_add_f32 v[90:91], v[90:91], v[228:229]
	v_pk_add_f32 v[84:85], v[176:177], v[232:233]
	v_pk_fma_f32 v[72:73], v[72:73], s[10:11], v[82:83] op_sel_hi:[1,0,1]
	v_pk_fma_f32 v[78:79], v[94:95], s[10:11], v[78:79] op_sel_hi:[1,0,1]
	v_pk_fma_f32 v[82:83], v[148:149], s[10:11], v[92:93] op_sel_hi:[1,0,1]
	v_pk_fma_f32 v[92:93], v[150:151], s[10:11], v[132:133] op_sel_hi:[1,0,1]
	v_pk_add_f32 v[94:95], v[154:155], v[246:247]
	v_pk_add_f32 v[64:65], v[76:77], v[64:65]
	v_pk_fma_f32 v[74:75], v[74:75], s[10:11], v[140:141] op_sel_hi:[1,0,1]
	v_pk_fma_f32 v[132:133], v[160:161], s[10:11], v[138:139] op_sel_hi:[1,0,1]
	v_pk_fma_f32 v[138:139], v[162:163], s[10:11], v[146:147] op_sel_hi:[1,0,1]
	v_pk_fma_f32 v[140:141], v[164:165], s[10:11], v[196:197] op_sel_hi:[1,0,1]
	v_pk_fma_f32 v[66:67], v[166:167], s[10:11], v[66:67] op_sel_hi:[1,0,1]
	v_pk_fma_f32 v[68:69], v[80:81], s[10:11], v[68:69] op_sel_hi:[1,0,1]
	v_cvt_pk_f32_fp8_sdwa v[156:157], v252 src0_sel:WORD_1
	v_pk_mul_f32 v[88:89], v[88:89], s[8:9] op_sel_hi:[1,0]
	v_pk_add_f32 v[238:239], v[238:239], 0 op_sel_hi:[1,0]
	v_pk_add_f32 v[90:91], v[90:91], v[234:235]
	v_pk_fma_f32 v[80:81], v[84:85], s[10:11], v[86:87] op_sel_hi:[1,0,1]
	v_pk_fma_f32 v[86:87], v[94:95], s[10:11], v[136:137] op_sel_hi:[1,0,1]
	v_pk_fma_f32 v[64:65], v[64:65], s[10:11], v[134:135] op_sel_hi:[1,0,1]
	v_add_f32_e32 v131, v140, v141
	v_add_f32_e32 v134, v138, v139
	v_add_f32_e32 v135, v68, v69
	v_add_f32_e32 v136, v66, v67
	v_pk_add_f32 v[158:159], v[238:239], v[242:243]
	v_pk_fma_f32 v[84:85], v[90:91], s[10:11], v[88:89] op_sel_hi:[1,0,1]
	v_add_f32_e32 v88, v78, v79
	v_add_f32_e32 v89, v72, v73
	v_add_f32_e32 v131, v134, v131
	v_add_f32_e32 v134, v136, v135
	v_pk_add_f32 v[158:159], v[158:159], v[244:245]
	v_add_f32_e32 v88, v89, v88
	v_add_f32_e32 v89, v84, v85
	v_add_f32_e32 v137, v80, v81
	v_add_f32_e32 v134, 0, v134
	v_pk_mul_f32 v[142:143], v[142:143], s[8:9] op_sel_hi:[1,0]
	v_pk_add_f32 v[76:77], v[158:159], v[152:153]
	v_add_f32_e32 v90, v92, v93
	v_add_f32_e32 v91, v82, v83
	v_add_f32_e32 v89, v137, v89
	v_add_f32_e32 v88, v134, v88
	v_pk_mul_f32 v[144:145], v[144:145], s[8:9] op_sel_hi:[1,0]
	v_pk_add_f32 v[70:71], v[70:71], v[156:157]
	v_pk_fma_f32 v[76:77], v[76:77], s[10:11], v[142:143] op_sel_hi:[1,0,1]
	v_add_f32_e32 v90, v91, v90
	v_add_f32_e32 v91, v64, v65
	v_add_f32_e32 v142, v86, v87
	v_add_f32_e32 v88, v88, v89
	v_pk_fma_f32 v[70:71], v[70:71], s[10:11], v[144:145] op_sel_hi:[1,0,1]
	v_add_f32_e32 v94, v132, v133
	v_add_f32_e32 v95, v74, v75
	v_add_f32_e32 v91, v142, v91
	v_add_f32_e32 v88, v88, v90
	v_add_f32_e32 v94, v95, v94
	v_add_f32_e32 v95, v70, v71
	v_add_f32_e32 v143, v76, v77
	v_add_f32_e32 v88, v88, v91
	v_add_f32_e32 v95, v143, v95
	v_add_f32_e32 v88, v88, v94
	v_add_f32_e32 v88, v88, v95
	v_add_f32_e32 v88, v88, v131
	s_nop 1
	v_add_f32_dpp v88, v88, v88 quad_perm:[1,0,3,2] row_mask:0xf bank_mask:0xf bound_ctrl:1
	s_nop 1
	v_add_f32_dpp v88, v88, v88 quad_perm:[2,3,0,1] row_mask:0xf bank_mask:0xf bound_ctrl:1
	s_nop 1
	v_add_f32_dpp v88, v88, v88 row_half_mirror row_mask:0xf bank_mask:0xf bound_ctrl:1
	s_nop 1
	v_add_f32_dpp v88, v88, v88 row_mirror row_mask:0xf bank_mask:0xf bound_ctrl:1
	v_mov_b32_e32 v89, v88
	s_nop 1
	v_permlane16_swap_b32_e32 v88, v89
	v_add_f32_e32 v88, v88, v89
	v_mov_b32_e32 v89, v88
	s_nop 1
	v_permlane32_swap_b32_e32 v88, v89
	v_add_f32_e32 v88, v88, v89
	v_fmac_f32_e32 v69, 0xba000000, v88
	v_fmac_f32_e32 v67, 0xba000000, v88
	v_fmac_f32_e32 v79, 0xba000000, v88
	v_fmac_f32_e32 v73, 0xba000000, v88
	v_fmamk_f32 v68, v88, 0xba000000, v68
	v_fmamk_f32 v66, v88, 0xba000000, v66
	v_fmamk_f32 v78, v88, 0xba000000, v78
	v_fmamk_f32 v72, v88, 0xba000000, v72
	v_fmamk_f32 v84, v88, 0xba000000, v84
	v_fmac_f32_e32 v85, 0xba000000, v88
	v_fmamk_f32 v80, v88, 0xba000000, v80
	v_fmac_f32_e32 v81, 0xba000000, v88
	v_fmamk_f32 v92, v88, 0xba000000, v92
	v_fmac_f32_e32 v93, 0xba000000, v88
	v_fmamk_f32 v82, v88, 0xba000000, v82
	v_fmac_f32_e32 v83, 0xba000000, v88
	v_fmamk_f32 v64, v88, 0xba000000, v64
	v_fmac_f32_e32 v65, 0xba000000, v88
	v_fmamk_f32 v86, v88, 0xba000000, v86
	v_fmac_f32_e32 v87, 0xba000000, v88
	v_fmamk_f32 v132, v88, 0xba000000, v132
	v_fmac_f32_e32 v133, 0xba000000, v88
	v_fmamk_f32 v74, v88, 0xba000000, v74
	v_fmac_f32_e32 v75, 0xba000000, v88
	v_fmamk_f32 v70, v88, 0xba000000, v70
	v_fmac_f32_e32 v71, 0xba000000, v88
	v_fmamk_f32 v76, v88, 0xba000000, v76
	v_fmac_f32_e32 v77, 0xba000000, v88
	v_fmamk_f32 v140, v88, 0xba000000, v140
	v_fmac_f32_e32 v141, 0xba000000, v88
	v_fmamk_f32 v138, v88, 0xba000000, v138
	v_fmac_f32_e32 v139, 0xba000000, v88
	v_mul_f32_e32 v88, v67, v67
	v_mul_f32_e32 v89, v69, v69
	v_mul_f32_e32 v90, v73, v73
	v_mul_f32_e32 v91, v79, v79
	v_mul_f32_e32 v94, v81, v81
	v_mul_f32_e32 v95, v85, v85
	v_fmac_f32_e32 v88, v66, v66
	v_fmac_f32_e32 v89, v68, v68
	v_fmac_f32_e32 v90, v72, v72
	v_fmac_f32_e32 v91, v78, v78
	v_mul_f32_e32 v131, v83, v83
	v_mul_f32_e32 v134, v93, v93
	v_fmac_f32_e32 v94, v80, v80
	v_fmac_f32_e32 v95, v84, v84
	v_add_f32_e32 v88, v88, v89
	v_add_f32_e32 v89, v90, v91
	v_mul_f32_e32 v135, v87, v87
	v_mul_f32_e32 v136, v65, v65
	v_fmac_f32_e32 v131, v82, v82
	v_fmac_f32_e32 v134, v92, v92
	v_add_f32_e32 v90, v94, v95
	v_add_f32_e32 v88, v88, v89
	v_mul_f32_e32 v137, v75, v75
	v_mul_f32_e32 v142, v133, v133
	v_fmac_f32_e32 v135, v86, v86
	v_fmac_f32_e32 v136, v64, v64
	v_add_f32_e32 v91, v131, v134
	v_add_f32_e32 v88, v88, v90
	v_mul_f32_e32 v143, v77, v77
	v_mul_f32_e32 v144, v71, v71
	v_fmac_f32_e32 v137, v74, v74
	v_fmac_f32_e32 v142, v132, v132
	v_add_f32_e32 v94, v135, v136
	v_add_f32_e32 v88, v88, v91
	v_mul_f32_e32 v145, v139, v139
	v_mul_f32_e32 v146, v141, v141
	v_fmac_f32_e32 v143, v76, v76
	v_fmac_f32_e32 v144, v70, v70
	v_add_f32_e32 v95, v137, v142
	v_add_f32_e32 v88, v88, v94
	v_fmac_f32_e32 v145, v138, v138
	v_fmac_f32_e32 v146, v140, v140
	v_add_f32_e32 v131, v143, v144
	v_add_f32_e32 v88, v88, v95
	v_add_f32_e32 v134, v145, v146
	v_add_f32_e32 v88, v88, v131
	v_add_f32_e32 v88, v88, v134
	s_nop 1
	v_add_f32_dpp v88, v88, v88 quad_perm:[1,0,3,2] row_mask:0xf bank_mask:0xf bound_ctrl:1
	s_nop 1
	v_add_f32_dpp v88, v88, v88 quad_perm:[2,3,0,1] row_mask:0xf bank_mask:0xf bound_ctrl:1
	s_nop 1
	v_add_f32_dpp v88, v88, v88 row_half_mirror row_mask:0xf bank_mask:0xf bound_ctrl:1
	s_nop 1
	v_add_f32_dpp v88, v88, v88 row_mirror row_mask:0xf bank_mask:0xf bound_ctrl:1
	v_mov_b32_e32 v89, v88
	s_nop 1
	v_permlane16_swap_b32_e32 v88, v89
	v_add_f32_e32 v88, v88, v89
	v_mov_b32_e32 v89, v88
	s_nop 1
	v_permlane32_swap_b32_e32 v88, v89
	v_add_f32_e32 v88, v88, v89
	v_fmamk_f32 v88, v88, 0x3a000000, v127
	v_mul_f32_e32 v89, 0x4f800000, v88
	v_cmp_gt_f32_e32 vcc, s20, v88
	s_nop 1
	v_cndmask_b32_e32 v88, v88, v89, vcc
	v_sqrt_f32_e32 v89, v88
	s_nop 0
	v_add_u32_e32 v90, -1, v89
	v_add_u32_e32 v91, 1, v89
	v_fma_f32 v94, -v90, v89, v88
	v_fma_f32 v95, -v91, v89, v88
	v_cmp_ge_f32_e64 s[2:3], 0, v94
	s_nop 1
	v_cndmask_b32_e64 v89, v89, v90, s[2:3]
	v_cmp_lt_f32_e64 s[2:3], 0, v95
	s_nop 1
	v_cndmask_b32_e64 v89, v89, v91, s[2:3]
	v_mul_f32_e32 v90, 0x37800000, v89
	v_cndmask_b32_e32 v89, v89, v90, vcc
	v_cmp_class_f32_e32 vcc, v88, v128
	s_nop 1
	v_cndmask_b32_e32 v88, v89, v88, vcc
	v_div_scale_f32 v89, s[2:3], v88, v88, 1.0
	v_rcp_f32_e32 v91, v89
	v_div_scale_f32 v90, vcc, 1.0, v88, 1.0
	v_fma_f32 v94, -v89, v91, 1.0
	v_fmac_f32_e32 v91, v94, v91
	v_mul_f32_e32 v94, v90, v91
	v_fma_f32 v95, -v89, v94, v90
	v_fmac_f32_e32 v94, v95, v91
	v_fma_f32 v89, -v89, v94, v90
	v_div_fmas_f32 v89, v89, v91, v94
	v_div_fixup_f32 v88, v89, v88, 1.0
	v_pk_mul_f32 v[66:67], v[88:89], v[66:67] op_sel_hi:[0,1]
	v_pk_mul_f32 v[68:69], v[88:89], v[68:69] op_sel_hi:[0,1]
	v_pk_mul_f32 v[72:73], v[88:89], v[72:73] op_sel_hi:[0,1]
	v_pk_mul_f32 v[78:79], v[88:89], v[78:79] op_sel_hi:[0,1]
	v_pk_mul_f32 v[80:81], v[88:89], v[80:81] op_sel_hi:[0,1]
	v_pk_mul_f32 v[84:85], v[88:89], v[84:85] op_sel_hi:[0,1]
	v_pk_mul_f32 v[82:83], v[88:89], v[82:83] op_sel_hi:[0,1]
	v_pk_mul_f32 v[90:91], v[88:89], v[92:93] op_sel_hi:[0,1]
	v_pk_mul_f32 v[86:87], v[88:89], v[86:87] op_sel_hi:[0,1]
	v_pk_mul_f32 v[64:65], v[88:89], v[64:65] op_sel_hi:[0,1]
	v_pk_mul_f32 v[74:75], v[88:89], v[74:75] op_sel_hi:[0,1]
	v_pk_mul_f32 v[92:93], v[88:89], v[132:133] op_sel_hi:[0,1]
	v_pk_mul_f32 v[76:77], v[88:89], v[76:77] op_sel_hi:[0,1]
	v_pk_mul_f32 v[70:71], v[88:89], v[70:71] op_sel_hi:[0,1]
	v_pk_mul_f32 v[94:95], v[88:89], v[140:141] op_sel_hi:[0,1]
	v_pk_mul_f32 v[88:89], v[88:89], v[138:139] op_sel_hi:[0,1]
	s_waitcnt lgkmcnt(13)
	v_pk_fma_f32 v[18:19], v[68:69], v[18:19], v[50:51]
	v_pk_fma_f32 v[16:17], v[66:67], v[16:17], v[48:49]
	s_mov_b64 vcc, s[0:1]
	s_waitcnt lgkmcnt(12)
	v_pk_fma_f32 v[2:3], v[78:79], v[2:3], v[34:35]
	v_pk_fma_f32 v[0:1], v[72:73], v[0:1], v[32:33]
	s_waitcnt lgkmcnt(9)
	v_pk_fma_f32 v[22:23], v[84:85], v[22:23], v[54:55]
	v_pk_fma_f32 v[20:21], v[80:81], v[20:21], v[52:53]
	s_waitcnt lgkmcnt(8)
	v_pk_fma_f32 v[6:7], v[90:91], v[6:7], v[38:39]
	v_pk_fma_f32 v[4:5], v[82:83], v[4:5], v[36:37]
	s_waitcnt lgkmcnt(5)
	v_pk_fma_f32 v[26:27], v[64:65], v[26:27], v[58:59]
	v_pk_fma_f32 v[24:25], v[86:87], v[24:25], v[56:57]
	s_waitcnt lgkmcnt(4)
	v_pk_fma_f32 v[10:11], v[92:93], v[10:11], v[42:43]
	v_pk_fma_f32 v[8:9], v[74:75], v[8:9], v[40:41]
	s_waitcnt lgkmcnt(1)
	v_pk_fma_f32 v[30:31], v[70:71], v[30:31], v[62:63]
	v_pk_fma_f32 v[28:29], v[76:77], v[28:29], v[60:61]
	s_waitcnt lgkmcnt(0)
	v_pk_fma_f32 v[12:13], v[88:89], v[12:13], v[44:45]
	v_pk_fma_f32 v[14:15], v[94:95], v[14:15], v[46:47]
	global_store_dwordx4 v[116:117], v[16:19], off sc0 sc1
	global_store_dwordx4 v[116:117], v[0:3], off offset:1024 sc0 sc1
	global_store_dwordx4 v[116:117], v[20:23], off offset:2048 sc0 sc1
	global_store_dwordx4 v[116:117], v[4:7], off offset:3072 sc0 sc1
	global_store_dwordx4 v[118:119], v[24:27], off sc0 sc1
	global_store_dwordx4 v[120:121], v[8:11], off sc0 sc1
	global_store_dwordx4 v[122:123], v[28:31], off sc0 sc1
	global_store_dwordx4 v[124:125], v[12:15], off sc0 sc1
	s_cbranch_vccnz .LBB0_1205
